# speedup vs baseline: 1.0189x; 1.0017x over previous
_Z7k_finalPKfS0_S0_Pf:
	s_load_dwordx8 s[4:11], s[0:1], 0x0
	s_lshl_b32 s2, s2, 4
	v_lshrrev_b32_e32 v1, 3, v0
	v_or_b32_e32 v34, s2, v1
	v_bfe_u32 v1, v0, 2, 1
	s_ashr_i32 s0, s2, 3
	v_bfe_u32 v35, v0, 1, 1
	s_and_b32 s0, s0, -4
	v_lshlrev_b32_e32 v2, 1, v1
	v_lshlrev_b32_e32 v3, 4, v34
	v_and_b32_e32 v50, 1, v0
	v_or3_b32 v2, s0, v2, v35
	v_and_b32_e32 v3, 0x1f0, v3
	v_lshl_or_b32 v36, v50, 9, v3
	v_mov_b32_e32 v37, 0
	v_ashrrev_i32_e32 v3, 31, v2
	s_waitcnt lgkmcnt(0)
	v_lshl_add_u64 v[4:5], s[4:5], 0, v[36:37]
	v_lshlrev_b64 v[2:3], 10, v[2:3]
	v_lshl_add_u64 v[30:31], v[4:5], 0, v[2:3]
	s_mov_b32 s0, 0x80000
	v_add_co_u32_e32 v6, vcc, s0, v30
	s_mov_b32 s0, 0x100000
	s_nop 0
	v_addc_co_u32_e32 v7, vcc, 0, v31, vcc
	v_add_co_u32_e32 v14, vcc, s0, v30
	s_mov_b32 s0, 0x180000
	s_nop 0
	v_addc_co_u32_e32 v15, vcc, 0, v31, vcc
	v_add_co_u32_e32 v16, vcc, s0, v30
	s_mov_b32 s0, 0x200000
	s_nop 0
	v_addc_co_u32_e32 v17, vcc, 0, v31, vcc
	global_load_dwordx4 v[22:25], v[30:31], off
	global_load_dwordx4 v[2:5], v[6:7], off
	global_load_dwordx4 v[10:13], v[14:15], off
	s_nop 0
	global_load_dwordx4 v[6:9], v[16:17], off
	v_add_co_u32_e32 v26, vcc, s0, v30
	s_mov_b32 s0, 0x280000
	s_nop 0
	v_addc_co_u32_e32 v27, vcc, 0, v31, vcc
	v_add_co_u32_e32 v28, vcc, s0, v30
	s_mov_b32 s0, 0x300000
	s_nop 0
	v_addc_co_u32_e32 v29, vcc, 0, v31, vcc
	global_load_dwordx4 v[18:21], v[26:27], off
	global_load_dwordx4 v[14:17], v[28:29], off
	v_add_co_u32_e32 v26, vcc, s0, v30
	s_mov_b32 s0, 0x380000
	s_nop 0
	v_addc_co_u32_e32 v27, vcc, 0, v31, vcc
	v_add_co_u32_e32 v30, vcc, s0, v30
	global_load_dwordx4 v[26:29], v[26:27], off
	s_nop 0
	v_addc_co_u32_e32 v31, vcc, 0, v31, vcc
	global_load_dwordx4 v[30:33], v[30:31], off
	v_lshlrev_b32_e32 v36, 6, v35
	v_and_or_b32 v44, v0, 15, s2
	v_mov_b32_e32 v45, v37
	v_mov_b32_e32 v49, v37
	v_lshl_or_b32 v1, v1, 7, v36
	v_add_u32_e32 v48, 0x6000, v44
	v_mov_b32_e32 v39, v37
	v_mov_b32_e32 v41, v37
	v_mov_b32_e32 v43, v37
	v_mov_b32_e32 v47, v37
	v_add_u32_e32 v38, 0x1000, v44
	v_add_u32_e32 v40, 0x2000, v44
	v_add_u32_e32 v42, 0x4000, v44
	v_add_u32_e32 v46, 0x5000, v44
	v_lshl_or_b32 v36, v50, 4, v1
	v_lshl_add_u64 v[50:51], v[44:45], 2, s[8:9]
	v_lshl_add_u64 v[48:49], v[48:49], 2, s[8:9]
	v_lshl_add_u64 v[52:53], v[38:39], 2, s[8:9]
	v_lshl_add_u64 v[54:55], v[40:41], 2, s[8:9]
	v_lshl_add_u64 v[56:57], v[42:43], 2, s[8:9]
	v_lshl_add_u64 v[46:47], v[46:47], 2, s[8:9]
	global_load_dword v40, v[50:51], off
	global_load_dword v42, v[52:53], off
	global_load_dword v38, v[54:55], off
	global_load_dword v41, v[56:57], off
	global_load_dword v43, v[46:47], off
	global_load_dword v39, v[48:49], off
	v_ashrrev_i32_e32 v35, 31, v34
	v_lshlrev_b64 v[62:63], 8, v[34:35]
	v_lshl_add_u64 v[62:63], s[6:7], 0, v[62:63]
	v_lshl_add_u64 v[62:63], v[62:63], 0, v[36:37]
	global_load_dwordx4 v[64:67], v[62:63], off
	global_load_dwordx4 v[68:71], v[62:63], off offset:32
	v_add_u32_e32 v72, 0x3000, v44
	v_mov_b32_e32 v73, 0
	v_lshl_add_u64 v[72:73], v[72:73], 2, s[8:9]
	global_load_dword v76, v[72:73], off
	v_add_u32_e32 v74, 0x7000, v44
	v_mov_b32_e32 v75, 0
	v_lshl_add_u64 v[74:75], v[74:75], 2, s[8:9]
	global_load_dword v77, v[74:75], off
	s_mov_b64 s[0:1], 0x8000
	s_waitcnt vmcnt(17)
	v_cvt_f32_f16_e32 v58, v22
	s_waitcnt vmcnt(15)
	v_cvt_f32_f16_e32 v48, v10
	v_cvt_f32_f16_sdwa v49, v10 dst_sel:DWORD dst_unused:UNUSED_PAD src0_sel:WORD_1
	s_waitcnt vmcnt(14)
	v_cvt_f32_f16_e32 v50, v6
	v_cvt_f32_f16_sdwa v51, v6 dst_sel:DWORD dst_unused:UNUSED_PAD src0_sel:WORD_1
	v_cvt_f32_f16_e32 v10, v11
	v_cvt_f32_f16_sdwa v11, v11 dst_sel:DWORD dst_unused:UNUSED_PAD src0_sel:WORD_1
	v_cvt_f32_f16_e32 v6, v7
	v_cvt_f32_f16_sdwa v7, v7 dst_sel:DWORD dst_unused:UNUSED_PAD src0_sel:WORD_1
	v_cvt_f32_f16_sdwa v59, v22 dst_sel:DWORD dst_unused:UNUSED_PAD src0_sel:WORD_1
	v_cvt_f32_f16_e32 v60, v2
	v_cvt_f32_f16_sdwa v61, v2 dst_sel:DWORD dst_unused:UNUSED_PAD src0_sel:WORD_1
	v_cvt_f32_f16_e32 v22, v23
	v_cvt_f32_f16_sdwa v23, v23 dst_sel:DWORD dst_unused:UNUSED_PAD src0_sel:WORD_1
	v_cvt_f32_f16_e32 v2, v3
	v_cvt_f32_f16_sdwa v3, v3 dst_sel:DWORD dst_unused:UNUSED_PAD src0_sel:WORD_1
	s_waitcnt vmcnt(12)
	v_cvt_f32_f16_e32 v54, v14
	v_cvt_f32_f16_sdwa v55, v14 dst_sel:DWORD dst_unused:UNUSED_PAD src0_sel:WORD_1
	v_pk_add_f32 v[6:7], v[10:11], v[6:7]
	v_cvt_f32_f16_e32 v10, v19
	v_cvt_f32_f16_sdwa v11, v19 dst_sel:DWORD dst_unused:UNUSED_PAD src0_sel:WORD_1
	v_cvt_f32_f16_e32 v14, v15
	v_cvt_f32_f16_sdwa v15, v15 dst_sel:DWORD dst_unused:UNUSED_PAD src0_sel:WORD_1
	v_pk_add_f32 v[2:3], v[22:23], v[2:3]
	v_pk_add_f32 v[46:47], v[58:59], v[60:61]
	v_cvt_f32_f16_e32 v52, v18
	v_cvt_f32_f16_sdwa v53, v18 dst_sel:DWORD dst_unused:UNUSED_PAD src0_sel:WORD_1
	s_waitcnt vmcnt(11)
	v_cvt_f32_f16_e32 v56, v26
	v_cvt_f32_f16_sdwa v57, v26 dst_sel:DWORD dst_unused:UNUSED_PAD src0_sel:WORD_1
	s_waitcnt vmcnt(10)
	v_cvt_f32_f16_e32 v58, v30
	v_cvt_f32_f16_sdwa v59, v30 dst_sel:DWORD dst_unused:UNUSED_PAD src0_sel:WORD_1
	v_pk_add_f32 v[2:3], v[2:3], v[6:7]
	v_pk_add_f32 v[6:7], v[10:11], v[14:15]
	v_cvt_f32_f16_e32 v10, v27
	v_cvt_f32_f16_sdwa v11, v27 dst_sel:DWORD dst_unused:UNUSED_PAD src0_sel:WORD_1
	v_cvt_f32_f16_e32 v14, v31
	v_cvt_f32_f16_sdwa v15, v31 dst_sel:DWORD dst_unused:UNUSED_PAD src0_sel:WORD_1
	v_pk_add_f32 v[48:49], v[48:49], v[50:51]
	v_pk_add_f32 v[50:51], v[56:57], v[58:59]
	v_pk_add_f32 v[46:47], v[46:47], v[48:49]
	v_pk_add_f32 v[48:49], v[52:53], v[54:55]
	v_pk_add_f32 v[10:11], v[10:11], v[14:15]
	v_pk_add_f32 v[48:49], v[48:49], v[50:51]
	v_pk_add_f32 v[6:7], v[6:7], v[10:11]
	v_add_u32_e32 v50, 0x3000, v44
	v_add_u32_e32 v22, 0x7000, v44
	v_pk_add_f32 v[44:45], v[46:47], v[48:49]
	v_pk_add_f32 v[46:47], v[2:3], v[6:7]
	v_cvt_f32_f16_e32 v6, v24
	v_cvt_f32_f16_sdwa v7, v24 dst_sel:DWORD dst_unused:UNUSED_PAD src0_sel:WORD_1
	v_cvt_f32_f16_e32 v10, v4
	v_cvt_f32_f16_sdwa v11, v4 dst_sel:DWORD dst_unused:UNUSED_PAD src0_sel:WORD_1
	v_cvt_f32_f16_e32 v14, v12
	v_cvt_f32_f16_sdwa v15, v12 dst_sel:DWORD dst_unused:UNUSED_PAD src0_sel:WORD_1
	v_cvt_f32_f16_e32 v26, v8
	v_cvt_f32_f16_sdwa v27, v8 dst_sel:DWORD dst_unused:UNUSED_PAD src0_sel:WORD_1
	v_pk_add_f32 v[6:7], v[6:7], v[10:11]
	v_mov_b32_e32 v51, v37
	v_lshl_add_u64 v[18:19], v[50:51], 2, s[8:9]
	v_pk_add_f32 v[10:11], v[14:15], v[26:27]
	v_cvt_f32_f16_e32 v14, v16
	v_pk_add_f32 v[10:11], v[6:7], v[10:11]
	v_cvt_f32_f16_e32 v6, v20
	v_cvt_f32_f16_sdwa v7, v20 dst_sel:DWORD dst_unused:UNUSED_PAD src0_sel:WORD_1
	v_cvt_f32_f16_sdwa v15, v16 dst_sel:DWORD dst_unused:UNUSED_PAD src0_sel:WORD_1
	v_mov_b32_e32 v23, v37
	v_lshl_add_u64 v[22:23], v[22:23], 2, s[8:9]
	v_lshlrev_b64 v[18:19], 8, v[34:35]
	v_pk_add_f32 v[14:15], v[6:7], v[14:15]
	v_lshl_add_u64 v[6:7], s[6:7], 0, v[18:19]
	v_cvt_f32_f16_e32 v26, v25
	v_cvt_f32_f16_sdwa v27, v25 dst_sel:DWORD dst_unused:UNUSED_PAD src0_sel:WORD_1
	v_cvt_f32_f16_e32 v22, v28
	v_cvt_f32_f16_sdwa v23, v28 dst_sel:DWORD dst_unused:UNUSED_PAD src0_sel:WORD_1
	v_cvt_f32_f16_e32 v24, v32
	v_cvt_f32_f16_sdwa v25, v32 dst_sel:DWORD dst_unused:UNUSED_PAD src0_sel:WORD_1
	v_lshl_add_u64 v[30:31], v[6:7], 0, v[36:37]
	v_cvt_f32_f16_e32 v48, v5
	v_cvt_f32_f16_sdwa v49, v5 dst_sel:DWORD dst_unused:UNUSED_PAD src0_sel:WORD_1
	v_pk_add_f32 v[22:23], v[22:23], v[24:25]
	v_cvt_f32_f16_e32 v12, v13
	v_pk_add_f32 v[14:15], v[14:15], v[22:23]
	v_cvt_f32_f16_sdwa v13, v13 dst_sel:DWORD dst_unused:UNUSED_PAD src0_sel:WORD_1
	v_cvt_f32_f16_e32 v8, v9
	v_cvt_f32_f16_sdwa v9, v9 dst_sel:DWORD dst_unused:UNUSED_PAD src0_sel:WORD_1
	v_pk_add_f32 v[10:11], v[10:11], v[14:15]
	v_pk_add_f32 v[14:15], v[26:27], v[48:49]
	v_cvt_f32_f16_e32 v20, v21
	v_cvt_f32_f16_sdwa v21, v21 dst_sel:DWORD dst_unused:UNUSED_PAD src0_sel:WORD_1
	v_cvt_f32_f16_e32 v16, v17
	v_cvt_f32_f16_sdwa v17, v17 dst_sel:DWORD dst_unused:UNUSED_PAD src0_sel:WORD_1
	v_cvt_f32_f16_e32 v26, v29
	v_cvt_f32_f16_sdwa v27, v29 dst_sel:DWORD dst_unused:UNUSED_PAD src0_sel:WORD_1
	v_cvt_f32_f16_e32 v28, v33
	v_cvt_f32_f16_sdwa v29, v33 dst_sel:DWORD dst_unused:UNUSED_PAD src0_sel:WORD_1
	v_pk_add_f32 v[8:9], v[12:13], v[8:9]
	v_pk_add_f32 v[12:13], v[20:21], v[16:17]
	v_pk_add_f32 v[8:9], v[14:15], v[8:9]
	v_pk_add_f32 v[14:15], v[26:27], v[28:29]
	v_and_b32_e32 v16, 7, v0
	v_pk_add_f32 v[12:13], v[12:13], v[14:15]
	s_waitcnt vmcnt(3)
	v_mul_f32_e32 v1, v65, v45
	v_fmac_f32_e32 v1, v64, v44
	v_mbcnt_lo_u32_b32 v4, -1, 0
	v_fmac_f32_e32 v1, v66, v46
	v_mbcnt_hi_u32_b32 v14, -1, v4
	v_fmac_f32_e32 v1, v67, v47
	v_and_b32_e32 v5, 64, v14
	s_waitcnt vmcnt(0)
	v_fmac_f32_e32 v1, v68, v10
	v_xor_b32_e32 v4, 1, v14
	v_add_u32_e32 v15, 64, v5
	v_pk_add_f32 v[12:13], v[8:9], v[12:13]
	v_fmac_f32_e32 v1, v69, v11
	v_cmp_lt_i32_e32 vcc, v4, v15
	v_fmac_f32_e32 v1, v70, v12
	v_fmac_f32_e32 v1, v71, v13
	v_cndmask_b32_e32 v4, v14, v4, vcc
	v_lshlrev_b32_e32 v4, 2, v4
	ds_bpermute_b32 v8, v4, v1
	v_lshl_add_u64 v[4:5], s[10:11], 0, v[18:19]
	v_lshl_add_u64 v[6:7], v[4:5], 0, v[36:37]
	v_xor_b32_e32 v4, 2, v14
	v_cmp_lt_i32_e32 vcc, v4, v15
	s_waitcnt lgkmcnt(0)
	v_add_f32_e32 v1, v1, v8
	v_lshl_add_u64 v[8:9], v[6:7], 0, s[0:1]
	v_cndmask_b32_e32 v4, v14, v4, vcc
	v_lshlrev_b32_e32 v4, 2, v4
	ds_bpermute_b32 v4, v4, v1
	s_mov_b32 s0, 0x8000
	s_waitcnt lgkmcnt(0)
	v_add_f32_e32 v1, v1, v4
	v_xor_b32_e32 v4, 4, v14
	v_cmp_lt_i32_e32 vcc, v4, v15
	s_nop 1
	v_cndmask_b32_e32 v4, v14, v4, vcc
	v_lshlrev_b32_e32 v4, 2, v4
	ds_bpermute_b32 v4, v4, v1
	v_add_co_u32_e32 v6, vcc, s0, v6
	s_nop 1
	v_addc_co_u32_e32 v7, vcc, 0, v7, vcc
	v_cmp_eq_u32_e32 vcc, 0, v16
	global_store_dwordx4 v[6:7], v[44:47], off sc1
	global_store_dwordx4 v[8:9], v[10:13], off offset:32 sc1
	s_and_saveexec_b64 s[0:1], vcc
	s_cbranch_execnz .LBB1_3
	s_or_b64 exec, exec, s[0:1]
	v_cmp_gt_u32_e32 vcc, 16, v0
	s_and_saveexec_b64 s[0:1], vcc
	s_cbranch_execnz .LBB1_4

.LBB1_4:
	s_waitcnt lgkmcnt(0)
	v_pk_add_f32 v[4:5], v[40:41], v[42:43]
	v_pk_add_f32 v[2:3], v[38:39], v[76:77]
	v_or_b32_e32 v0, s2, v0
	v_pk_add_f32 v[2:3], v[4:5], v[2:3]
	v_mov_b32_e32 v1, 0
	v_add_f32_e32 v2, v2, v3
	v_lshl_add_u64 v[0:1], v[0:1], 2, s[10:11]
	global_store_dword v[0:1], v2, off sc1
	s_endpgm
	s_nop 0
	s_nop 0
	s_nop 0
	s_nop 0
	s_nop 0
	s_nop 0
	s_nop 0
	s_nop 0
	s_nop 0
	s_nop 0
	s_nop 0
	s_nop 0
	s_nop 0
	s_nop 0
	s_nop 0
	s_endpgm

	.amdhsa_kernel _Z7k_finalPKfS0_S0_Pf
		.amdhsa_group_segment_fixed_size 0
		.amdhsa_private_segment_fixed_size 0
		.amdhsa_kernarg_size 32
		.amdhsa_user_sgpr_count 2
		.amdhsa_user_sgpr_dispatch_ptr 0
		.amdhsa_user_sgpr_queue_ptr 0
		.amdhsa_user_sgpr_kernarg_segment_ptr 1
		.amdhsa_user_sgpr_dispatch_id 0
		.amdhsa_user_sgpr_kernarg_preload_length 0
		.amdhsa_user_sgpr_kernarg_preload_offset 0
		.amdhsa_user_sgpr_private_segment_size 0
		.amdhsa_uses_dynamic_stack 0
		.amdhsa_enable_private_segment 0
		.amdhsa_system_sgpr_workgroup_id_x 1
		.amdhsa_system_sgpr_workgroup_id_y 0
		.amdhsa_system_sgpr_workgroup_id_z 0
		.amdhsa_system_sgpr_workgroup_info 0
		.amdhsa_system_vgpr_workitem_id 0
		.amdhsa_next_free_vgpr 78
		.amdhsa_next_free_sgpr 12
		.amdhsa_accum_offset 80
		.amdhsa_reserve_vcc 1
		.amdhsa_float_round_mode_32 0
		.amdhsa_float_round_mode_16_64 0
		.amdhsa_float_denorm_mode_32 3
		.amdhsa_float_denorm_mode_16_64 3
		.amdhsa_dx10_clamp 1
		.amdhsa_ieee_mode 1
		.amdhsa_fp16_overflow 0
		.amdhsa_tg_split 0
		.amdhsa_exception_fp_ieee_invalid_op 0
		.amdhsa_exception_fp_denorm_src 0
		.amdhsa_exception_fp_ieee_div_zero 0
		.amdhsa_exception_fp_ieee_overflow 0
		.amdhsa_exception_fp_ieee_underflow 0
		.amdhsa_exception_fp_ieee_inexact 0
		.amdhsa_exception_int_div_zero 0
	.end_amdhsa_kernel

amdhsa.kernels:
  - .agpr_count:     16
    .args:
      - .actual_access:  read_only
        .address_space:  global
        .offset:         0
        .size:           8
        .value_kind:     global_buffer
      - .actual_access:  read_only
        .address_space:  global
        .offset:         8
        .size:           8
        .value_kind:     global_buffer
      - .actual_access:  read_only
        .address_space:  global
        .offset:         16
        .size:           8
        .value_kind:     global_buffer
      - .actual_access:  read_only
        .address_space:  global
        .offset:         24
        .size:           8
        .value_kind:     global_buffer
      - .actual_access:  write_only
        .address_space:  global
        .offset:         32
        .size:           8
        .value_kind:     global_buffer
      - .actual_access:  write_only
        .address_space:  global
        .offset:         40
        .size:           8
        .value_kind:     global_buffer
      - .actual_access:  write_only
        .address_space:  global
        .offset:         48
        .size:           8
        .value_kind:     global_buffer
      - .actual_access:  write_only
        .address_space:  global
        .offset:         56
        .size:           8
        .value_kind:     global_buffer
      - .actual_access:  read_only
        .address_space:  global
        .offset:         64
        .size:           8
        .value_kind:     global_buffer
      - .actual_access:  read_only
        .address_space:  global
        .offset:         72
        .size:           8
        .value_kind:     global_buffer
      - .actual_access:  read_only
        .address_space:  global
        .offset:         80
        .size:           8
        .value_kind:     global_buffer
    .group_segment_fixed_size: 33792
    .kernarg_segment_align: 8
    .kernarg_segment_size: 88
    .language:       OpenCL C
    .language_version:
      - 2
      - 0
    .max_flat_workgroup_size: 256
    .name:           _Z6k_prepPKfS0_S0_S0_PDF16_S1_S1_S1_S0_S0_S0_
    .private_segment_fixed_size: 0
    .sgpr_count:     22
    .sgpr_spill_count: 0
    .symbol:         _Z6k_prepPKfS0_S0_S0_PDF16_S1_S1_S1_S0_S0_S0_.kd
    .uniform_work_group_size: 1
    .uses_dynamic_stack: false
    .vgpr_count:     184
    .vgpr_spill_count: 0
    .wavefront_size: 64
  - .agpr_count:     0
    .args:
      - .actual_access:  read_only
        .address_space:  global
        .offset:         0
        .size:           8
        .value_kind:     global_buffer
      - .actual_access:  read_only
        .address_space:  global
        .offset:         8
        .size:           8
        .value_kind:     global_buffer
      - .actual_access:  read_only
        .address_space:  global
        .offset:         16
        .size:           8
        .value_kind:     global_buffer
      - .actual_access:  write_only
        .address_space:  global
        .offset:         24
        .size:           8
        .value_kind:     global_buffer
    .group_segment_fixed_size: 0
    .kernarg_segment_align: 8
    .kernarg_segment_size: 32
    .language:       OpenCL C
    .language_version:
      - 2
      - 0
    .max_flat_workgroup_size: 128
    .name:           _Z7k_finalPKfS0_S0_Pf
    .private_segment_fixed_size: 0
    .sgpr_count:     18
    .sgpr_spill_count: 0
    .symbol:         _Z7k_finalPKfS0_S0_Pf.kd
    .uniform_work_group_size: 1
    .uses_dynamic_stack: false
    .vgpr_count:     78
    .vgpr_spill_count: 0
    .wavefront_size: 64
  - .agpr_count:     0
    .args:
      - .actual_access:  read_only
        .address_space:  global
        .offset:         0
        .size:           8
        .value_kind:     global_buffer
      - .actual_access:  read_only
        .address_space:  global
        .offset:         8
        .size:           8
        .value_kind:     global_buffer
      - .actual_access:  read_only
        .address_space:  global
        .offset:         16
        .size:           8
        .value_kind:     global_buffer
      - .actual_access:  read_only
        .address_space:  global
        .offset:         24
        .size:           8
        .value_kind:     global_buffer
      - .actual_access:  read_only
        .address_space:  global
        .offset:         32
        .size:           8
        .value_kind:     global_buffer
      - .actual_access:  write_only
        .address_space:  global
        .offset:         40
        .size:           8
        .value_kind:     global_buffer
      - .actual_access:  write_only
        .address_space:  global
        .offset:         48
        .size:           8
        .value_kind:     global_buffer
      - .actual_access:  read_only
        .address_space:  global
        .offset:         56
        .size:           8
        .value_kind:     global_buffer
      - .actual_access:  read_only
        .address_space:  global
        .offset:         64
        .size:           8
        .value_kind:     global_buffer
    .group_segment_fixed_size: 33808
    .kernarg_segment_align: 8
    .kernarg_segment_size: 72
    .language:       OpenCL C
    .language_version:
      - 2
      - 0
    .max_flat_workgroup_size: 384
    .name:           _Z6k_gemmILi0EEvPKDF16_S1_PKfS3_S1_PDF16_PfS1_S5_
    .private_segment_fixed_size: 0
    .sgpr_count:     20
    .sgpr_spill_count: 0
    .symbol:         _Z6k_gemmILi0EEvPKDF16_S1_PKfS3_S1_PDF16_PfS1_S5_.kd
    .uniform_work_group_size: 1
    .uses_dynamic_stack: false
    .vgpr_count:     150
    .vgpr_spill_count: 0
    .wavefront_size: 64
  - .agpr_count:     0
    .args:
      - .actual_access:  read_only
        .address_space:  global
        .offset:         0
        .size:           8
        .value_kind:     global_buffer
      - .actual_access:  read_only
        .address_space:  global
        .offset:         8
        .size:           8
        .value_kind:     global_buffer
      - .actual_access:  read_only
        .address_space:  global
        .offset:         16
        .size:           8
        .value_kind:     global_buffer
      - .actual_access:  read_only
        .address_space:  global
        .offset:         24
        .size:           8
        .value_kind:     global_buffer
      - .actual_access:  read_only
        .address_space:  global
        .offset:         32
        .size:           8
        .value_kind:     global_buffer
      - .actual_access:  read_only
        .address_space:  global
        .offset:         40
        .size:           8
        .value_kind:     global_buffer
      - .actual_access:  read_only
        .address_space:  global
        .offset:         48
        .size:           8
        .value_kind:     global_buffer
      - .actual_access:  read_only
        .address_space:  global
        .offset:         56
        .size:           8
        .value_kind:     global_buffer
      - .actual_access:  write_only
        .address_space:  global
        .offset:         64
        .size:           8
        .value_kind:     global_buffer
    .group_segment_fixed_size: 50176
    .kernarg_segment_align: 8
    .kernarg_segment_size: 72
    .language:       OpenCL C
    .language_version:
      - 2
      - 0
    .max_flat_workgroup_size: 384
    .name:           _Z6k_gemmILi1EEvPKDF16_S1_PKfS3_S1_PDF16_PfS1_S5_
    .private_segment_fixed_size: 0
    .sgpr_count:     20
    .sgpr_spill_count: 0
    .symbol:         _Z6k_gemmILi1EEvPKDF16_S1_PKfS3_S1_PDF16_PfS1_S5_.kd
    .uniform_work_group_size: 1
    .uses_dynamic_stack: false
    .vgpr_count:     182
    .vgpr_spill_count: 0
    .wavefront_size: 64
